# v86: M3 retention item top: decay tables and gate/norm-weight requests placed between the bulk load requests and their first counted wait
# baseline (speedup 1.0000x reference)
.LBB0_555:
	s_and_b32 s33, s3, 1
	s_lshl_b32 s4, s33, 1
	s_add_i32 s14, s4, s18
	s_mul_i32 s4, s10, 0x1100
	s_lshl_b32 s5, s11, 7
	s_add_i32 s45, s4, s5
	s_lshl_b32 s22, s14, 6
	v_or_b32_e32 v2, s45, v116
	v_mov_b64_e32 v[50:51], s[88:89]
	s_mul_i32 s5, s14, 0x44
	s_ashr_i32 s23, s22, 31
	v_mad_i64_i32 v[2:3], s[14:15], v2, s60, v[50:51]
	s_lshl_b64 s[14:15], s[22:23], 1
	v_mov_b32_e32 v101, v0
	v_lshl_add_u64 v[2:3], v[2:3], 0, s[14:15]
	v_or_b32_e32 v10, s45, v117
	v_lshl_add_u64 v[2:3], v[2:3], 0, v[100:101]
	v_mad_i64_i32 v[10:11], s[26:27], v10, s60, v[50:51]
	s_mul_i32 s4, s10, 0x110
	v_add_co_u32_e32 v6, vcc, s78, v2
	v_lshl_add_u64 v[10:11], v[10:11], 0, s[14:15]
	v_or_b32_e32 v18, s45, v118
	s_add_i32 s4, s4, s5
	v_addc_co_u32_e32 v7, vcc, 0, v3, vcc
	v_lshl_add_u64 v[10:11], v[10:11], 0, v[100:101]
	v_mad_i64_i32 v[18:19], s[26:27], v18, s60, v[50:51]
	s_add_i32 s4, s4, s11
	v_add_co_u32_e32 v14, vcc, s78, v10
	v_lshl_add_u64 v[18:19], v[18:19], 0, s[14:15]
	v_or_b32_e32 v26, s45, v119
	s_ashr_i32 s5, s4, 31
	v_addc_co_u32_e32 v15, vcc, 0, v11, vcc
	v_lshl_add_u64 v[18:19], v[18:19], 0, v[100:101]
	v_mad_i64_i32 v[26:27], s[26:27], v26, s60, v[50:51]
	s_lshl_b64 s[10:11], s[4:5], 13
	s_add_i32 s4, s4, 34
	v_add_co_u32_e32 v22, vcc, s78, v18
	v_lshl_add_u64 v[26:27], v[26:27], 0, s[14:15]
	s_ashr_i32 s5, s4, 31
	v_addc_co_u32_e32 v23, vcc, 0, v19, vcc
	v_lshl_add_u64 v[26:27], v[26:27], 0, v[100:101]
	s_lshl_b64 s[4:5], s[4:5], 13
	v_add_co_u32_e32 v30, vcc, s78, v26
	s_cmp_eq_u32 s33, 0
	s_nop 0
	v_addc_co_u32_e32 v31, vcc, 0, v27, vcc
	s_cselect_b64 vcc, -1, 0
	s_add_u32 s10, s66, s10
	s_addc_u32 s11, s67, s11
	s_add_u32 s4, s66, s4
	s_addc_u32 s5, s67, s5
	v_or_b32_e32 v104, s45, v109
	global_load_dwordx4 v[2:5], v[6:7], off offset:512
	s_nop 0
	global_load_dwordx4 v[6:9], v[6:7], off
	s_nop 0
	global_load_dwordx4 v[10:13], v[14:15], off offset:512
	s_nop 0
	global_load_dwordx4 v[14:17], v[14:15], off
	s_nop 0
	global_load_dwordx4 v[18:21], v[22:23], off offset:512
	s_nop 0
	global_load_dwordx4 v[22:25], v[22:23], off
	s_nop 0
	global_load_dwordx4 v[26:29], v[30:31], off offset:512
	s_nop 0
	global_load_dwordx4 v[30:33], v[30:31], off
	s_nop 0
	global_load_dwordx4 v[34:37], v125, s[10:11]
	global_load_dwordx4 v[38:41], v125, s[4:5]
	global_load_dwordx4 v[42:45], v126, s[10:11]
	global_load_dwordx4 v[46:49], v126, s[4:5]
	v_mad_i64_i32 v[106:107], s[4:5], v104, s60, v[50:51]
	v_lshl_add_u64 v[50:51], v[106:107], 0, s[14:15]
	v_mov_b32_e32 v103, v0
	v_lshl_add_u64 v[50:51], v[50:51], 0, v[102:103]
	global_load_dwordx4 v[78:81], v[50:51], off offset:3584
	global_load_dwordx4 v[74:77], v[50:51], off offset:3616
	global_load_dwordx4 v[70:73], v[50:51], off offset:3648
	global_load_dwordx4 v[66:69], v[50:51], off offset:3680
	v_cndmask_b32_e32 v50, v142, v1, vcc
	s_mov_b32 s10, 0
	v_mul_f32_e32 v101, 0xbfb8aa3b, v50
	v_ashrrev_i32_e32 v105, 31, v104
	s_mov_b64 s[4:5], -1
	v_cndmask_b32_e32 v152, v143, v141, vcc
	v_mul_f32_e32 v103, 0xbfb8aa3b, v152
	v_mul_f32_e32 v167, 0xbf800000, v101
	v_mul_f32_e32 v168, 0xc0000000, v101
	v_mul_f32_e32 v169, 0xc0400000, v101
	v_mul_f32_e32 v170, 0xc1000000, v101
	v_mul_f32_e32 v171, 0x3f800000, v103
	v_mul_f32_e32 v172, 0x40000000, v103
	v_mul_f32_e32 v173, 0x40400000, v103
	v_mul_f32_e32 v174, 0x41000000, v103
	v_exp_f32_e32 v167, v167
	v_exp_f32_e32 v168, v168
	v_exp_f32_e32 v169, v169
	v_exp_f32_e32 v170, v170
	v_exp_f32_e32 v171, v171
	v_exp_f32_e32 v172, v172
	v_exp_f32_e32 v173, v173
	v_exp_f32_e32 v174, v174
	v_lshl_add_u64 v[152:153], s[22:23], 1, v[106:107]
	v_lshlrev_b32_e32 v154, 1, v82
	v_mov_b32_e32 v155, v0
	v_lshl_add_u64 v[152:153], v[152:153], 0, v[154:155]
	s_mov_b64 s[98:99], 0x1400
	ds_read_b64 v[156:157], v0 offset:640
	v_lshl_add_u64 v[154:155], v[152:153], 0, s[98:99]
	v_add_co_u32_e32 v152, vcc, s78, v152
	s_lshl_b64 s[98:99], s[24:25], 2
	s_lshl_b64 s[100:101], s[22:23], 2
	v_addc_co_u32_e32 v153, vcc, 0, v153, vcc
	global_load_dwordx2 v[222:223], v[152:153], off offset:1024
	global_load_dwordx2 v[224:225], v[154:155], off offset:16
	global_load_dwordx2 v[226:227], v[154:155], off offset:32
	global_load_dwordx2 v[228:229], v[154:155], off offset:48
	global_load_dwordx2 v[230:231], v[154:155], off offset:64
	global_load_dwordx2 v[232:233], v[154:155], off offset:80
	global_load_dwordx2 v[234:235], v[154:155], off offset:96
	global_load_dwordx2 v[236:237], v[154:155], off offset:112
	s_add_u32 s98, s98, s100
	s_addc_u32 s99, s99, s101
	s_waitcnt lgkmcnt(0)
	v_readfirstlane_b32 s100, v156
	v_readfirstlane_b32 s101, v157
	v_lshlrev_b32_e32 v152, 2, v82
	s_add_u32 s98, s100, s98
	s_addc_u32 s99, s101, s99
	global_load_dwordx4 v[238:241], v152, s[98:99]
	global_load_dwordx4 v[242:245], v152, s[98:99] offset:32
	global_load_dwordx4 v[246:249], v152, s[98:99] offset:64
	global_load_dwordx4 v[250:253], v152, s[98:99] offset:96
	global_load_dwordx4 v[200:203], v152, s[98:99] offset:128
	global_load_dwordx4 v[204:207], v152, s[98:99] offset:160
	global_load_dwordx4 v[214:217], v152, s[98:99] offset:192
	global_load_dwordx4 v[192:195], v152, s[98:99] offset:224
	s_waitcnt vmcnt(31)
	ds_write_b128 v127, v[2:5]
	s_waitcnt vmcnt(30)
	ds_write_b128 v128, v[6:9] offset:16384
	s_waitcnt vmcnt(29)
	ds_write_b128 v129, v[10:13]
	s_waitcnt vmcnt(28)
	ds_write_b128 v130, v[14:17] offset:16384
	s_waitcnt vmcnt(27)
	ds_write_b128 v127, v[18:21] offset:8192
	s_waitcnt vmcnt(26)
	ds_write_b128 v131, v[22:25] offset:16384
	s_waitcnt vmcnt(25)
	ds_write_b128 v132, v[26:29] offset:8192
	s_waitcnt vmcnt(24)
	ds_write_b128 v133, v[30:33] offset:16384
	s_waitcnt vmcnt(23)
	ds_write_b128 v128, v[34:37] offset:32768
	s_waitcnt vmcnt(22)
	ds_write_b128 v128, v[38:41] offset:40960
	s_waitcnt vmcnt(21)
	ds_write_b128 v130, v[42:45] offset:32768
	s_waitcnt vmcnt(20)
	ds_write_b128 v130, v[46:49] offset:40960
	v_mov_b32_e32 v18, 0
	v_mov_b32_e32 v19, v18
	v_mov_b32_e32 v20, v18
	v_mov_b32_e32 v21, v18
	v_mov_b32_e32 v22, v18
	v_mov_b32_e32 v23, v18
	v_mov_b32_e32 v24, v18
	v_mov_b32_e32 v25, v18
	v_mov_b32_e32 v26, v18
	v_mov_b32_e32 v27, v18
	v_mov_b32_e32 v28, v18
	v_mov_b32_e32 v29, v18
	v_mov_b32_e32 v30, v18
	v_mov_b32_e32 v31, v18
	v_mov_b32_e32 v32, v18
	v_mov_b32_e32 v33, v18
	v_mov_b32_e32 v2, v18
	v_mov_b32_e32 v3, v18
	v_mov_b32_e32 v4, v18
	v_mov_b32_e32 v5, v18
	v_mov_b32_e32 v6, v18
	v_mov_b32_e32 v7, v18
	v_mov_b32_e32 v8, v18
	v_mov_b32_e32 v9, v18
	v_mov_b32_e32 v10, v18
	v_mov_b32_e32 v11, v18
	v_mov_b32_e32 v12, v18
	v_mov_b32_e32 v13, v18
	v_mov_b32_e32 v14, v18
	v_mov_b32_e32 v15, v18
	v_mov_b32_e32 v16, v18
	v_mov_b32_e32 v17, v18
	s_waitcnt lgkmcnt(0)
	s_barrier
